# rot-9 rotation plus counted vmcnt(7..4) in the first half of the loop-2 F copy
# baseline (speedup 1.0000x reference)
.Ll1_cont:
	ds_bpermute_b32 v2, v69, v84
	ds_bpermute_b32 v5, v69, v83
	v_max_f32_e32 v4, v84, v84
	v_max_f32_e32 v7, v83, v83
	ds_bpermute_b32 v3, v69, v63
	s_waitcnt lgkmcnt(2)
	v_max_f32_e32 v6, v2, v2
	v_max_f32_e32 v4, v4, v6
	v_sub_f32_e32 v6, v84, v4
	v_exp_f32_e32 v9, v6
	s_waitcnt lgkmcnt(1)
	v_max_f32_e32 v6, v5, v5
	v_sub_f32_e32 v2, v2, v4
	v_max_f32_e32 v6, v7, v6
	v_exp_f32_e32 v11, v2
	ds_bpermute_b32 v2, v69, v62
	v_sub_f32_e32 v5, v5, v6
	v_sub_f32_e32 v7, v83, v6
	v_exp_f32_e32 v10, v5
	v_exp_f32_e32 v8, v7
	v_cmp_gt_u32_e32 vcc, 32, v98
	s_waitcnt lgkmcnt(0)
	v_pk_mul_f32 v[2:3], v[10:11], v[2:3]
	s_nop 0
	v_pk_fma_f32 v[8:9], v[62:63], v[8:9], v[2:3]
	v_lshlrev_b32_e32 v2, 7, v184
	v_or3_b32 v10, v183, v2, v1
	s_and_saveexec_b64 s[0:1], vcc
	v_lshl_add_u32 v2, v10, 4, 0
	v_add_u32_e32 v2, 0x21000, v2
	v_mov_b32_e32 v5, v9
	v_mov_b32_e32 v7, v8
	ds_write_b128 v2, v[4:7]
	s_or_b64 exec, exec, s[0:1]
	s_lshl_b32 s12, s21, 7
	s_mov_b32 s3, 0
	v_or_b32_e32 v2, s12, v82
	s_lshl_b32 s13, s21, 11
	s_add_i32 s23, 0, 0x12000
	v_lshlrev_b32_e32 v2, 12, v2
	v_mov_b32_e32 v3, 0
	s_add_i32 s13, s13, s16
	s_lshl_b64 s[0:1], s[2:3], 13
	v_lshl_add_u64 v[12:13], s[14:15], 0, v[2:3]
	v_mov_b32_e32 v69, v3
	s_add_u32 s0, s10, s0
	v_lshl_add_u64 v[172:173], v[12:13], 0, v[68:69]
	s_addc_u32 s1, s11, s1
	s_lshl_b32 s10, s22, 7
	s_mov_b32 s11, s3
	s_waitcnt vmcnt(1)
	v_lshl_add_u64 v[36:37], v[172:173], 0, s[10:11]
	s_mov_b32 s10, 0x40000
	v_add_co_u32_e32 v38, vcc, s10, v36
	s_waitcnt lgkmcnt(0)
	s_barrier
	global_load_dwordx4 v[12:15], v[58:59], off
	global_load_dwordx4 v[16:19], v[70:71], off
	v_addc_co_u32_e32 v39, vcc, 0, v37, vcc
	global_load_dwordx4 v[20:23], v[56:57], off
	global_load_dwordx4 v[24:27], v[66:67], off
	global_load_dwordx4 v[28:31], v[36:37], off
	global_load_dwordx4 v[32:35], v[38:39], off
	v_add_f32_e32 v2, v78, v80
	s_movk_i32 s11, 0x1200
	v_add_f32_e32 v5, v79, v81
	s_mov_b32 s14, 0x3fb8aa3b
	v_lshlrev_b32_e32 v10, 4, v10
	v_mov_b32_e32 v36, s23
	v_mul_f32_e32 v37, 0x3fb8aa3b, v2
	v_mul_f32_e32 v38, 0x3fb8aa3b, v5
	v_xor_b32_e32 v10, 0x800, v10
	v_mad_u32_u24 v40, v55, s11, v36
	v_fma_f32 v36, v2, s14, -v37
	v_rndne_f32_e32 v39, v37
	v_fma_f32 v41, v5, s14, -v38
	s_waitcnt vmcnt(6)
	v_rndne_f32_e32 v42, v38
	v_add_u32_e32 v10, 0, v10
	v_fmac_f32_e32 v36, 0x32a5705f, v2
	v_sub_f32_e32 v37, v37, v39
	v_fmac_f32_e32 v41, 0x32a5705f, v5
	v_sub_f32_e32 v38, v38, v42
	v_add_u32_e32 v10, 0x21000, v10
	v_add_f32_e32 v44, v37, v36
	global_load_dwordx4 v[146:149], v[60:61], off
	global_load_dwordx4 v[150:153], v[64:65], off
	v_cvt_i32_f32_e32 v43, v39
	v_add_f32_e32 v41, v38, v41
	ds_read_b128 v[36:39], v10
	v_exp_f32_e32 v10, v44
	v_cvt_i32_f32_e32 v42, v42
	v_exp_f32_e32 v41, v41
	s_mov_b32 s21, 0xc2ce8ed0
	s_lshl_b32 s11, s20, 6
	s_add_i32 s14, s11, 64
	v_ldexp_f32 v10, v10, v43
	v_cmp_ngt_f32_e32 vcc, s21, v2
	s_mov_b32 s22, 0x42b17218
	s_and_b32 s14, s14, 0x7c0
	v_ldexp_f32 v41, v41, v42
	v_cndmask_b32_e32 v10, 0, v10, vcc
	v_cmp_ngt_f32_e32 vcc, s21, v5
	v_mov_b32_e32 v7, 0x7f800000
	v_max_f32_e32 v11, v4, v4
	s_mov_b32 s15, s3
	s_lshl_b32 s14, s14, 1
	s_waitcnt lgkmcnt(0)
	v_max_f32_e32 v42, v36, v36
	v_cndmask_b32_e32 v41, 0, v41, vcc
	v_cmp_nlt_f32_e32 vcc, s22, v2
	v_max_f32_e32 v187, v11, v42
	v_mov_b32_e32 v55, v3
	v_cndmask_b32_e32 v2, v7, v10, vcc
	v_cmp_nlt_f32_e32 vcc, s22, v5
	v_lshl_add_u64 v[10:11], v[172:173], 0, s[14:15]
	v_lshl_add_u64 v[178:179], s[0:1], 0, v[54:55]
	v_cndmask_b32_e32 v5, v7, v41, vcc
	v_sub_f32_e32 v2, v2, v5
	v_add_f32_e32 v41, 0x3e4ccccd, v2
	v_sub_f32_e32 v2, v4, v187
	v_max_f32_e32 v4, v6, v6
	s_and_b32 s1, s2, 7
	s_mulk_i32 s1, 0x480
	s_mulk_i32 s19, 0x240
	s_add_i32 s0, s20, 2
	s_waitcnt vmcnt(7)
	ds_write_b128 v185, v[12:15]
	s_waitcnt vmcnt(6)
	ds_write_b128 v185, v[16:19] offset:9216
	s_waitcnt vmcnt(5)
	ds_write_b128 v185, v[20:23] offset:18432
	s_waitcnt vmcnt(4)
	ds_write_b128 v185, v[24:27] offset:27648
	s_waitcnt vmcnt(3)
	ds_write_b128 v185, v[28:31] offset:36864
	s_waitcnt vmcnt(2)
	ds_write_b128 v185, v[32:35] offset:46080
	v_add_co_u32_e32 v12, vcc, s10, v10
	v_exp_f32_e32 v23, v2
	s_nop 0
	v_addc_co_u32_e32 v13, vcc, 0, v11, vcc
	global_load_dwordx4 v[154:157], v[10:11], off
	global_load_dwordx4 v[158:161], v[12:13], off
	s_waitcnt lgkmcnt(0)
	s_barrier
	ds_read_b128 v[10:13], v186
	v_sub_f32_e32 v2, v36, v187
	v_exp_f32_e32 v25, v2
	v_max_f32_e32 v2, v38, v38
	v_max_f32_e32 v188, v4, v2
	v_sub_f32_e32 v2, v6, v188
	v_exp_f32_e32 v22, v2
	v_sub_f32_e32 v2, v38, v188
	v_exp_f32_e32 v24, v2
	ds_read_b128 v[14:17], v186 offset:9216
	ds_read_b128 v[18:21], v186 offset:32
	s_waitcnt lgkmcnt(2)
	v_mfma_f32_32x32x16_f16 v[66:81], v[10:13], v[114:117], 0
	v_mov_b32_e32 v36, v39
	v_mul_f32_e64 v10, v36, v24
	v_mul_f32_e64 v11, v37, v25
	ds_read_b128 v[4:7], v186 offset:9248
	s_add_i32 s1, s1, s19
	s_mov_b32 s14, 0x30000
	s_mov_b32 s15, 0x80000
	s_mov_b32 s19, 0
	s_waitcnt lgkmcnt(2)
	v_mfma_f32_32x32x16_f16 v[82:97], v[14:17], v[130:133], 0
	v_fma_f32 v16, v8, v22, v10
	v_fma_f32 v17, v9, v23, v11
	v_log_f32_e32 v238, v17
	s_nop 0
	v_add_f32_e32 v187, v187, v238
	v_sub_f32_e32 v240, 0, v187
	v_sub_f32_e32 v241, 0, v187
	v_sub_f32_e32 v242, 0, v187
	v_sub_f32_e32 v243, 0, v187
	v_sub_f32_e32 v244, 0, v187
	v_sub_f32_e32 v245, 0, v187
	v_sub_f32_e32 v246, 0, v187
	v_sub_f32_e32 v247, 0, v187
	v_sub_f32_e32 v248, 0, v187
	v_sub_f32_e32 v249, 0, v187
	v_sub_f32_e32 v250, 0, v187
	v_sub_f32_e32 v251, 0, v187
	v_sub_f32_e32 v252, 0, v187
	v_sub_f32_e32 v253, 0, v187
	v_sub_f32_e32 v254, 0, v187
	v_sub_f32_e32 v255, 0, v187
	v_lshrrev_b32_e32 v22, 3, v98
	v_or3_b32 v2, s13, v183, v22
	v_lshlrev_b64 v[8:9], 13, v[2:3]
	v_lshl_add_u64 v[8:9], s[4:5], 0, v[8:9]
	v_lshlrev_b32_e32 v2, 2, v101
	v_lshl_add_u64 v[8:9], v[8:9], 0, v[2:3]
	v_and_b32_e32 v2, 0x70, v54
	v_lshl_add_u64 v[174:175], v[8:9], 0, v[2:3]
	ds_read_b128 v[8:11], v186 offset:64
	s_waitcnt lgkmcnt(2)
	v_mfma_f32_32x32x16_f16 v[66:81], v[18:21], v[118:121], v[66:81]
	v_div_scale_f32 v18, s[4:5], v16, v16, -v41
	v_rcp_f32_e32 v19, v18
	v_div_scale_f32 v20, vcc, -v41, v16, -v41
	s_mov_b32 s13, 0x20000
	v_mov_b32_e32 v24, v3
	s_waitcnt lgkmcnt(1)
	v_mfma_f32_32x32x16_f16 v[82:97], v[4:7], v[134:137], v[82:97]
	v_fma_f32 v4, -v18, v19, 1.0
	v_fmac_f32_e32 v19, v4, v19
	v_mul_f32_e32 v21, v20, v19
	ds_read_b128 v[4:7], v186 offset:9280
	ds_read_b128 v[12:15], v186 offset:96
	v_mov_b32_e32 v25, v3
	v_mov_b32_e32 v26, v3
	v_mov_b32_e32 v27, v3
	s_waitcnt lgkmcnt(2)
	v_mfma_f32_32x32x16_f16 v[66:81], v[8:11], v[122:125], v[66:81]
	v_fma_f32 v8, -v18, v21, v20
	v_fmac_f32_e32 v21, v8, v19
	v_fma_f32 v18, -v18, v21, v20
	v_div_scale_f32 v20, s[4:5], v17, v17, 1.0
	v_rcp_f32_e32 v23, v20
	ds_read_b128 v[8:11], v186 offset:9312
	s_waitcnt lgkmcnt(2)
	v_mfma_f32_32x32x16_f16 v[82:97], v[4:7], v[138:141], v[82:97]
	v_div_fmas_f32 v4, v18, v19, v21
	v_div_fixup_f32 v176, v4, v16, -v41
	v_fma_f32 v4, -v20, v23, 1.0
	v_fmac_f32_e32 v23, v4, v23
	v_div_scale_f32 v4, vcc, 1.0, v17, 1.0
	v_mul_f32_e32 v5, v4, v23
	v_fma_f32 v6, -v20, v5, v4
	v_fmac_f32_e32 v5, v6, v23
	s_waitcnt lgkmcnt(1)
	v_mfma_f32_32x32x16_f16 v[66:81], v[12:15], v[126:129], v[66:81]
	v_fma_f32 v4, -v20, v5, v4
	v_div_fmas_f32 v4, v4, v23, v5
	v_div_fixup_f32 v177, v4, v17, 1.0
	v_mul_u32_u24_e32 v4, 0x90, v22
	v_add3_u32 v189, v40, v4, v2
	v_mul_u32_u24_e32 v2, 0x90, v1
	v_lshlrev_b32_e32 v4, 2, v99
	s_waitcnt lgkmcnt(0)
	v_mfma_f32_32x32x16_f16 v[82:97], v[8:11], v[142:145], v[82:97]
	v_add3_u32 v190, v40, v2, v4
	v_mul_u32_u24_e32 v2, 0x48, v1
	v_lshl_add_u32 v2, v2, 1, 0
	v_lshlrev_b32_e32 v4, 1, v101
	v_add3_u32 v191, v2, v4, v100
	s_mov_b32 s4, 0x3f800000
	s_mov_b32 s5, 0x10000
	v_mov_b32_e32 v2, v3
	v_mov_b32_e32 v4, v3
	v_mov_b32_e32 v5, v3
	v_mov_b32_e32 v6, v3
	v_mov_b32_e32 v7, v3
	v_mov_b32_e32 v8, v3
	v_mov_b32_e32 v9, v3
	v_mov_b32_e32 v10, v3
	v_mov_b32_e32 v11, v3
	v_mov_b32_e32 v12, v3
	v_mov_b32_e32 v13, v3
	v_mov_b32_e32 v14, v3
	v_mov_b32_e32 v15, v3
	v_mov_b32_e32 v16, v3
	v_mov_b32_e32 v17, v3
	v_mov_b32_e32 v18, v3
	v_mov_b32_e32 v19, v3
	v_mov_b32_e32 v20, v3
	v_mov_b32_e32 v21, v3
	v_mov_b32_e32 v22, v3
	v_mov_b32_e32 v23, v3
	v_mov_b32_e32 v28, v3
	v_mov_b32_e32 v29, v3
	v_mov_b32_e32 v30, v3
	v_mov_b32_e32 v31, v3
	v_mov_b32_e32 v32, v3
	v_mov_b32_e32 v33, v3
	v_mov_b32_e32 v34, v3
	v_mov_b32_e32 v35, v3
	v_mov_b32_e32 v36, v3
	v_mov_b32_e32 v37, v3
	v_mov_b32_e32 v38, v3
	v_mov_b32_e32 v39, v3
	v_mov_b32_e32 v40, v3
	v_mov_b32_e32 v41, v3
	v_mov_b32_e32 v42, v3
	v_mov_b32_e32 v43, v3
	v_mov_b32_e32 v44, v3
	v_mov_b32_e32 v45, v3
	v_mov_b32_e32 v46, v3
	v_mov_b32_e32 v47, v3
	v_mov_b32_e32 v48, v3
	v_mov_b32_e32 v49, v3
	v_mov_b32_e32 v50, v3
	v_mov_b32_e32 v51, v3
	v_mov_b32_e32 v52, v3
	v_mov_b32_e32 v53, v3
	v_mov_b32_e32 v54, v3
	v_mov_b32_e32 v56, v3
	v_mov_b32_e32 v57, v3
	v_mov_b32_e32 v58, v3
	v_mov_b32_e32 v59, v3
	v_mov_b32_e32 v60, v3
	v_mov_b32_e32 v61, v3
	v_mov_b32_e32 v62, v3
	v_mov_b32_e32 v63, v3
	v_mov_b32_e32 v64, v3
	v_mov_b32_e32 v65, v3
	v_add_u32_e32 v192, 0xd800, v191
	v_sub_f32_e32 v66, v66, v187
	v_sub_f32_e32 v67, v67, v187
	v_sub_f32_e32 v68, v68, v187
	v_sub_f32_e32 v69, v69, v187
	v_sub_f32_e32 v70, v70, v187
	v_sub_f32_e32 v71, v71, v187
	v_sub_f32_e32 v72, v72, v187
	v_sub_f32_e32 v73, v73, v187
	v_sub_f32_e32 v74, v74, v187
	v_sub_f32_e32 v75, v75, v187
	v_sub_f32_e32 v76, v76, v187
	v_sub_f32_e32 v77, v77, v187
	v_sub_f32_e32 v78, v78, v187
	v_sub_f32_e32 v79, v79, v187
	v_sub_f32_e32 v80, v80, v187
	v_sub_f32_e32 v81, v81, v187
	s_mov_b32 s27, 0x42c80000
	v_cmp_gt_f32_e64 vcc, |v188|, s27
	s_cbranch_vccnz .Ll2_gen
	v_sub_f32_e32 v238, 0, v188
	v_exp_f32_e32 v238, v238
	s_nop 0
	v_mul_f32_e32 v176, v176, v238
	s_waitcnt vmcnt(0)
	s_barrier
	s_branch .Ll2f_top
